# speedup vs baseline: 1.0024x; 1.0024x over previous
.Lk_144:
	v_or_b32_e32 v46, 0x400, v54
	buffer_load_dwordx4 v[46:49], v46, s[4:7], 0 offen sc1
	ds_read_b128 v[50:53], v1
	v_mov_b32_e32 v66, 0
	v_add_u32_e32 v63, 0x800, v54
	s_mov_b32 s9, 0
	v_mov_b32_e32 v67, 0
	v_mov_b32_e32 v68, 0
	v_mov_b32_e32 v62, 0xc038aa3b
	s_mov_b32 s8, 0x4038aa3b
	v_mov_b32_e32 v65, 0
	v_mov_b32_e32 v64, v66
	s_setprio 2
	v_mov_b32_e32 v92, 0xc038aa3b
	v_mov_b32_e32 v93, 0xc038aa3b
	s_mov_b32 s8, 0x4038aa3b
	s_mov_b32 s9, 0
	v_mov_b32_e32 v64, 0
	v_mov_b32_e32 v65, 0
	v_mov_b32_e32 v66, 0
	v_mov_b32_e32 v67, 0
	v_mov_b32_e32 v68, 0
	v_mov_b32_e32 v116, v1
	v_mov_b32_e32 v117, v63
	s_mov_b32 s12, 0
	s_waitcnt lgkmcnt(0)
	s_setprio 2
	v_mfma_f32_16x16x32_f16 v[84:87], v[6:9], v[50:53], v[18:21]
	v_mfma_f32_16x16x32_f16 v[88:91], v[10:13], v[50:53], v[38:41]
	ds_read_b128 v[56:59], v75 offset:2048
	ds_read_b128 v[60:63], v75 offset:3072
	s_waitcnt vmcnt(1)
	v_mfma_f32_16x16x32_f16 v[84:87], v[2:5], v[42:45], v[84:87]
	v_mfma_f32_16x16x32_f16 v[88:91], v[14:17], v[42:45], v[88:91]
	s_waitcnt lgkmcnt(1)
	v_mfma_f32_16x16x32_f16 v[84:87], v[30:33], v[56:59], v[84:87]
	v_mfma_f32_16x16x32_f16 v[88:91], v[22:25], v[56:59], v[88:91]
	s_waitcnt lgkmcnt(0)
	v_mfma_f32_16x16x32_f16 v[84:87], v[34:37], v[60:63], v[84:87]
	v_mfma_f32_16x16x32_f16 v[88:91], v[26:29], v[60:63], v[88:91]
	s_nop 7
	s_setprio 0
	v_exp_f32_e32 v94, v86
	v_exp_f32_e32 v95, v90
	v_exp_f32_e32 v96, v84
	v_exp_f32_e32 v97, v88
	v_exp_f32_e32 v98, v85
	v_exp_f32_e32 v99, v89
	v_pk_add_f32 v[100:101], v[94:95], 1.0 op_sel_hi:[1,0]
	v_pk_fma_f32 v[102:103], v[94:95], s[8:9], v[92:93] op_sel_hi:[1,0,0]
	v_pk_fma_f32 v[100:101], v[96:97], v[100:101], v[100:101]
	v_pk_fma_f32 v[104:105], v[100:101], v[98:99], v[100:101]
	v_rcp_f32_e32 v104, v104
	v_rcp_f32_e32 v105, v105
	v_pk_fma_f32 v[102:103], v[102:103], v[98:99], v[102:103]
	v_pk_fma_f32 v[102:103], v[64:65], v[100:101], v[102:103]
	v_exp_f32_e32 v106, v87
	v_pk_mul_f32 v[64:65], v[102:103], v[104:105]
	v_exp_f32_e32 v108, v64
	v_exp_f32_e32 v109, v65
	v_exp_f32_e32 v107, v91
	v_pk_add_f32 v[110:111], v[108:109], 1.0 op_sel_hi:[1,0]
	v_pk_fma_f32 v[110:111], v[110:111], v[106:107], v[110:111]
	v_rcp_f32_e32 v110, v110
	v_rcp_f32_e32 v111, v111
	v_pk_add_f32 v[112:113], v[108:109], -1.0 op_sel_hi:[1,0]
	v_pk_mul_f32 v[112:113], v[112:113], v[110:111]
	v_cvt_pk_f16_f32 v114, v112, v113
	ds_write_b32 v81, v114 offset:0
	s_waitcnt lgkmcnt(0)
	global_load_dword v67, v66, s[0:1] sc1
	global_load_dword v68, v66, s[0:1] offset:4 sc1
	s_add_u32 s13, s12, 3
	s_min_u32 s13, s13, 450
	s_cmp_ge_u32 s14, s13
	s_cbranch_scc0 .Lca_slow_3
.Lca_ok_1:
	buffer_load_dwordx4 v[42:45], v117, s[4:7], 0 offen offset:0 sc1
	ds_read_b128 v[50:53], v116 offset:256
	s_setprio 0
	s_waitcnt vmcnt(3) lgkmcnt(0)
	s_setprio 2
	s_barrier
	v_mfma_f32_16x16x32_f16 v[84:87], v[6:9], v[50:53], v[18:21]
	v_mfma_f32_16x16x32_f16 v[88:91], v[10:13], v[50:53], v[38:41]
	ds_read_b128 v[56:59], v75 offset:0
	ds_read_b128 v[60:63], v75 offset:1024
	v_mfma_f32_16x16x32_f16 v[84:87], v[2:5], v[46:49], v[84:87]
	v_mfma_f32_16x16x32_f16 v[88:91], v[14:17], v[46:49], v[88:91]
	s_waitcnt lgkmcnt(1)
	v_mfma_f32_16x16x32_f16 v[84:87], v[30:33], v[56:59], v[84:87]
	v_mfma_f32_16x16x32_f16 v[88:91], v[22:25], v[56:59], v[88:91]
	s_waitcnt lgkmcnt(0)
	v_mfma_f32_16x16x32_f16 v[84:87], v[34:37], v[60:63], v[84:87]
	v_mfma_f32_16x16x32_f16 v[88:91], v[26:29], v[60:63], v[88:91]
	s_nop 7
	s_setprio 0
	v_exp_f32_e32 v94, v86
	v_exp_f32_e32 v95, v90
	v_exp_f32_e32 v96, v84
	v_exp_f32_e32 v97, v88
	v_exp_f32_e32 v98, v85
	v_exp_f32_e32 v99, v89
	v_pk_add_f32 v[100:101], v[94:95], 1.0 op_sel_hi:[1,0]
	v_pk_fma_f32 v[102:103], v[94:95], s[8:9], v[92:93] op_sel_hi:[1,0,0]
	v_pk_fma_f32 v[100:101], v[96:97], v[100:101], v[100:101]
	v_pk_fma_f32 v[104:105], v[100:101], v[98:99], v[100:101]
	v_rcp_f32_e32 v104, v104
	v_rcp_f32_e32 v105, v105
	v_pk_fma_f32 v[102:103], v[102:103], v[98:99], v[102:103]
	v_pk_fma_f32 v[102:103], v[64:65], v[100:101], v[102:103]
	v_exp_f32_e32 v106, v87
	v_pk_mul_f32 v[64:65], v[102:103], v[104:105]
	v_exp_f32_e32 v108, v64
	v_exp_f32_e32 v109, v65
	v_exp_f32_e32 v107, v91
	v_pk_add_f32 v[110:111], v[108:109], 1.0 op_sel_hi:[1,0]
	v_pk_fma_f32 v[110:111], v[110:111], v[106:107], v[110:111]
	v_rcp_f32_e32 v110, v110
	v_rcp_f32_e32 v111, v111
	v_pk_add_f32 v[112:113], v[108:109], -1.0 op_sel_hi:[1,0]
	v_pk_mul_f32 v[112:113], v[112:113], v[110:111]
	v_cvt_pk_f16_f32 v114, v112, v113
	ds_write_b32 v81, v114 offset:2048
	s_waitcnt lgkmcnt(0)
	s_add_u32 s13, s12, 4
	s_min_u32 s13, s13, 450
	s_cmp_ge_u32 s14, s13
	s_cbranch_scc0 .Lca_slow_6
.Lca_ok_4:
	buffer_load_dwordx4 v[46:49], v117, s[4:7], 0 offen offset:1024 sc1
	ds_read_b128 v[50:53], v116 offset:512
	s_setprio 0
	s_waitcnt vmcnt(1) lgkmcnt(0)
	v_add_u32_e32 v116, 0x200, v116
	v_add_u32_e32 v117, 0x800, v117
	s_mov_b32 s12, 2
	.p2align	6
.Lca_loop:
	s_setprio 2
	s_barrier
	v_mfma_f32_16x16x32_f16 v[84:87], v[6:9], v[50:53], v[18:21]
	v_mfma_f32_16x16x32_f16 v[88:91], v[10:13], v[50:53], v[38:41]
	ds_read_b128 v[56:59], v75 offset:2048
	ds_read_b128 v[60:63], v75 offset:3072
	v_mfma_f32_16x16x32_f16 v[84:87], v[2:5], v[42:45], v[84:87]
	v_mfma_f32_16x16x32_f16 v[88:91], v[14:17], v[42:45], v[88:91]
	s_waitcnt lgkmcnt(1)
	v_mfma_f32_16x16x32_f16 v[84:87], v[30:33], v[56:59], v[84:87]
	v_mfma_f32_16x16x32_f16 v[88:91], v[22:25], v[56:59], v[88:91]
	s_waitcnt lgkmcnt(0)
	v_mfma_f32_16x16x32_f16 v[84:87], v[34:37], v[60:63], v[84:87]
	v_mfma_f32_16x16x32_f16 v[88:91], v[26:29], v[60:63], v[88:91]
	s_nop 7
	s_setprio 0
	v_min_f32_e32 v64, 0x42700000, v64
	v_min_f32_e32 v65, 0x42700000, v65
	v_exp_f32_e32 v94, v86
	v_exp_f32_e32 v95, v90
	v_exp_f32_e32 v96, v84
	v_exp_f32_e32 v97, v88
	v_exp_f32_e32 v98, v85
	v_exp_f32_e32 v99, v89
	v_pk_add_f32 v[100:101], v[94:95], 1.0 op_sel_hi:[1,0]
	v_pk_fma_f32 v[102:103], v[94:95], s[8:9], v[92:93] op_sel_hi:[1,0,0]
	v_pk_fma_f32 v[100:101], v[96:97], v[100:101], v[100:101]
	v_pk_fma_f32 v[104:105], v[100:101], v[98:99], v[100:101]
	v_rcp_f32_e32 v104, v104
	v_rcp_f32_e32 v105, v105
	v_pk_fma_f32 v[102:103], v[102:103], v[98:99], v[102:103]
	v_pk_fma_f32 v[102:103], v[64:65], v[100:101], v[102:103]
	v_exp_f32_e32 v106, v87
	v_pk_mul_f32 v[64:65], v[102:103], v[104:105]
	v_exp_f32_e32 v108, v64
	v_exp_f32_e32 v109, v65
	v_exp_f32_e32 v107, v91
	v_pk_add_f32 v[110:111], v[108:109], 1.0 op_sel_hi:[1,0]
	v_pk_fma_f32 v[110:111], v[110:111], v[106:107], v[110:111]
	v_rcp_f32_e32 v110, v110
	v_rcp_f32_e32 v111, v111
	v_pk_add_f32 v[112:113], v[108:109], -1.0 op_sel_hi:[1,0]
	v_pk_mul_f32 v[112:113], v[112:113], v[110:111]
	v_cvt_pk_f16_f32 v114, v112, v113
	ds_write_b32 v81, v114 offset:0
	s_waitcnt lgkmcnt(0)
	v_readfirstlane_b32 s10, v67
	v_readfirstlane_b32 s11, v68
	global_load_dword v67, v66, s[0:1] sc1
	global_load_dword v68, v66, s[0:1] offset:4 sc1
	s_min_u32 s10, s10, s11
	s_max_u32 s14, s14, s10
	s_add_u32 s13, s12, 3
	s_min_u32 s13, s13, 450
	s_cmp_ge_u32 s14, s13
	s_cbranch_scc0 .Lca_slow_9

.Lca_ok_10:
	buffer_load_dwordx4 v[46:49], v117, s[4:7], 0 offen offset:1024 sc1
	ds_read_b128 v[50:53], v116 offset:512
	s_setprio 0
	s_waitcnt vmcnt(1) lgkmcnt(0)
	s_setprio 2
	s_barrier
	v_mfma_f32_16x16x32_f16 v[84:87], v[6:9], v[50:53], v[18:21]
	v_mfma_f32_16x16x32_f16 v[88:91], v[10:13], v[50:53], v[38:41]
	ds_read_b128 v[56:59], v75 offset:2048
	ds_read_b128 v[60:63], v75 offset:3072
	v_mfma_f32_16x16x32_f16 v[84:87], v[2:5], v[42:45], v[84:87]
	v_mfma_f32_16x16x32_f16 v[88:91], v[14:17], v[42:45], v[88:91]
	s_waitcnt lgkmcnt(1)
	v_mfma_f32_16x16x32_f16 v[84:87], v[30:33], v[56:59], v[84:87]
	v_mfma_f32_16x16x32_f16 v[88:91], v[22:25], v[56:59], v[88:91]
	s_waitcnt lgkmcnt(0)
	v_mfma_f32_16x16x32_f16 v[84:87], v[34:37], v[60:63], v[84:87]
	v_mfma_f32_16x16x32_f16 v[88:91], v[26:29], v[60:63], v[88:91]
	s_nop 7
	s_setprio 0
	v_exp_f32_e32 v94, v86
	v_exp_f32_e32 v95, v90
	v_exp_f32_e32 v96, v84
	v_exp_f32_e32 v97, v88
	v_exp_f32_e32 v98, v85
	v_exp_f32_e32 v99, v89
	v_pk_add_f32 v[100:101], v[94:95], 1.0 op_sel_hi:[1,0]
	v_pk_fma_f32 v[102:103], v[94:95], s[8:9], v[92:93] op_sel_hi:[1,0,0]
	v_pk_fma_f32 v[100:101], v[96:97], v[100:101], v[100:101]
	v_pk_fma_f32 v[104:105], v[100:101], v[98:99], v[100:101]
	v_rcp_f32_e32 v104, v104
	v_rcp_f32_e32 v105, v105
	v_pk_fma_f32 v[102:103], v[102:103], v[98:99], v[102:103]
	v_pk_fma_f32 v[102:103], v[64:65], v[100:101], v[102:103]
	v_exp_f32_e32 v106, v87
	v_pk_mul_f32 v[64:65], v[102:103], v[104:105]
	v_exp_f32_e32 v108, v64
	v_exp_f32_e32 v109, v65
	v_exp_f32_e32 v107, v91
	v_pk_add_f32 v[110:111], v[108:109], 1.0 op_sel_hi:[1,0]
	v_pk_fma_f32 v[110:111], v[110:111], v[106:107], v[110:111]
	v_rcp_f32_e32 v110, v110
	v_rcp_f32_e32 v111, v111
	v_pk_add_f32 v[112:113], v[108:109], -1.0 op_sel_hi:[1,0]
	v_pk_mul_f32 v[112:113], v[112:113], v[110:111]
	v_cvt_pk_f16_f32 v114, v112, v113
	ds_write_b32 v81, v114 offset:0
	s_waitcnt lgkmcnt(0)
	v_readfirstlane_b32 s10, v67
	v_readfirstlane_b32 s11, v68
	global_load_dword v67, v66, s[0:1] sc1
	global_load_dword v68, v66, s[0:1] offset:4 sc1
	s_min_u32 s10, s10, s11
	s_max_u32 s14, s14, s10
	s_add_u32 s13, s12, 5
	s_min_u32 s13, s13, 450
	s_cmp_ge_u32 s14, s13
	s_cbranch_scc0 .Lca_slow_15
.Lca_ok_13:
	buffer_load_dwordx4 v[42:45], v117, s[4:7], 0 offen offset:2048 sc1
	ds_read_b128 v[50:53], v116 offset:768
	s_setprio 0
	s_waitcnt vmcnt(3) lgkmcnt(0)
	s_setprio 2
	s_barrier
	v_mfma_f32_16x16x32_f16 v[84:87], v[6:9], v[50:53], v[18:21]
	v_mfma_f32_16x16x32_f16 v[88:91], v[10:13], v[50:53], v[38:41]
	ds_read_b128 v[56:59], v75 offset:0
	ds_read_b128 v[60:63], v75 offset:1024
	v_mfma_f32_16x16x32_f16 v[84:87], v[2:5], v[46:49], v[84:87]
	v_mfma_f32_16x16x32_f16 v[88:91], v[14:17], v[46:49], v[88:91]
	s_waitcnt lgkmcnt(1)
	v_mfma_f32_16x16x32_f16 v[84:87], v[30:33], v[56:59], v[84:87]
	v_mfma_f32_16x16x32_f16 v[88:91], v[22:25], v[56:59], v[88:91]
	s_waitcnt lgkmcnt(0)
	v_mfma_f32_16x16x32_f16 v[84:87], v[34:37], v[60:63], v[84:87]
	v_mfma_f32_16x16x32_f16 v[88:91], v[26:29], v[60:63], v[88:91]
	s_nop 7
	s_setprio 0
	v_exp_f32_e32 v94, v86
	v_exp_f32_e32 v95, v90
	v_exp_f32_e32 v96, v84
	v_exp_f32_e32 v97, v88
	v_exp_f32_e32 v98, v85
	v_exp_f32_e32 v99, v89
	v_pk_add_f32 v[100:101], v[94:95], 1.0 op_sel_hi:[1,0]
	v_pk_fma_f32 v[102:103], v[94:95], s[8:9], v[92:93] op_sel_hi:[1,0,0]
	v_pk_fma_f32 v[100:101], v[96:97], v[100:101], v[100:101]
	v_pk_fma_f32 v[104:105], v[100:101], v[98:99], v[100:101]
	v_rcp_f32_e32 v104, v104
	v_rcp_f32_e32 v105, v105
	v_pk_fma_f32 v[102:103], v[102:103], v[98:99], v[102:103]
	v_pk_fma_f32 v[102:103], v[64:65], v[100:101], v[102:103]
	v_exp_f32_e32 v106, v87
	v_pk_mul_f32 v[64:65], v[102:103], v[104:105]
	v_exp_f32_e32 v108, v64
	v_exp_f32_e32 v109, v65
	v_exp_f32_e32 v107, v91
	v_pk_add_f32 v[110:111], v[108:109], 1.0 op_sel_hi:[1,0]
	v_pk_fma_f32 v[110:111], v[110:111], v[106:107], v[110:111]
	v_rcp_f32_e32 v110, v110
	v_rcp_f32_e32 v111, v111
	v_pk_add_f32 v[112:113], v[108:109], -1.0 op_sel_hi:[1,0]
	v_pk_mul_f32 v[112:113], v[112:113], v[110:111]
	v_cvt_pk_f16_f32 v114, v112, v113
	ds_write_b32 v81, v114 offset:2048
	s_waitcnt lgkmcnt(0)
	s_add_u32 s13, s12, 6
	s_min_u32 s13, s13, 450
	s_cmp_ge_u32 s14, s13
	s_cbranch_scc0 .Lca_slow_18
.Lca_ok_16:
	buffer_load_dwordx4 v[46:49], v117, s[4:7], 0 offen offset:3072 sc1
	ds_read_b128 v[50:53], v116 offset:1024
	s_setprio 0
	s_waitcnt vmcnt(1) lgkmcnt(0)
	s_add_u32 s12, s12, 4
	v_add_u32_e32 v116, 0x400, v116
	v_add_u32_e32 v117, 0x1000, v117
	s_cmp_lt_u32 s12, 450
	s_cbranch_scc1 .Lca_loop
	s_barrier
	s_barrier
	s_barrier
	s_barrier
	s_endpgm
